# gather epilogue rewritten: gate and next-norm adaLN parameter vectors staged once per phase in LDS, per-token epilogue reads them from LDS instead of global
# speedup vs baseline: 1.1402x; 1.0243x over previous
.LBB0_1401:
	s_andn2_b64 vcc, exec, s[0:1]
	s_cbranch_vccnz .LBB0_1479
	s_mov_b64 s[36:37], s[30:31]
	s_waitcnt vmcnt(0)
	v_mbcnt_lo_u32_b32 v0, -1, 0
	v_mbcnt_hi_u32_b32 v0, -1, v0
	s_nop 0
	v_add_u32_e32 v0, s3, v0
	s_nop 0
	v_readfirstlane_b32 s0, v0
	s_ashr_i32 s0, s0, 6
	s_add_i32 s44, s0, s67
	s_cmpk_gt_i32 s44, 0x3fff
	s_cbranch_scc1 .LBB0_1427
	s_load_dwordx2 s[4:5], s[36:37], 0xd8
	s_mul_i32 s74, s11, 0x3000
	v_and_b32_e32 v80, 63, v0
	v_lshrrev_b32_e32 v0, 2, v0
	v_lshlrev_b32_e32 v96, 6, v80
	s_waitcnt lgkmcnt(0)
	s_add_u32 s46, s4, 0x372ac000
	s_addc_u32 s47, s5, 0
	s_add_u32 s48, s4, 0x37aac000
	s_addc_u32 s49, s5, 0
	s_lshl_b64 s[50:51], s[74:75], 2
	s_add_u32 s8, s4, s50
	s_addc_u32 s9, s5, s51
	s_add_u32 s6, s4, 0xbaac000
	s_addc_u32 s88, s5, 0
	s_add_u32 s89, s4, 0xeaac000
	s_addc_u32 s92, s5, 0
	s_add_u32 s93, s4, 0xaaac000
	s_addc_u32 s20, s5, 0
	s_lshl_b32 s0, s0, 11
	s_add_i32 s21, s0, 0
	s_cmp_lg_u32 s11, 3
	s_cselect_b64 s[52:53], -1, 0
	s_add_u32 s84, s4, 0x4000
	s_addc_u32 s82, s5, 0
	v_and_b32_e32 v83, 12, v0
	v_lshl_add_u64 v[0:1], s[4:5], 0, v[96:97]
	s_cmp_eq_u32 s11, 1
	s_mov_b64 s[0:1], 0x1eaac000
	s_mov_b64 s[14:15], 0x1aaac000
	s_cselect_b64 s[54:55], -1, 0
	s_cmp_lg_u32 s11, 1
	v_lshl_add_u64 v[86:87], v[0:1], 0, s[0:1]
	s_mov_b64 s[0:1], 0x12aac000
	v_lshlrev_b32_e32 v96, 7, v80
	v_lshlrev_b32_e32 v82, 5, v80
	v_lshl_add_u64 v[84:85], v[0:1], 0, s[14:15]
	s_cselect_b64 s[34:35], -1, 0
	s_lshl_b32 s74, s11, 11
	v_lshl_add_u64 v[94:95], v[0:1], 0, s[0:1]
	v_lshl_add_u64 v[0:1], s[8:9], 0, v[96:97]
	s_mov_b64 s[0:1], 0xe000
	v_lshlrev_b32_e32 v81, 4, v80
	v_or_b32_e32 v89, 64, v80
	v_lshl_add_u32 v91, v80, 3, s21
	v_or_b32_e32 v88, 8, v82
	v_or_b32_e32 v90, 16, v82
	v_or_b32_e32 v92, 24, v82
	v_lshl_add_u64 v[98:99], v[0:1], 0, s[0:1]
	s_add_i32 s83, s21, 0x420
	s_lshl_b64 s[28:29], s[74:75], 2
	v_add_u32_e32 v0, s3, v80
	v_lshlrev_b32_e32 v1, 4, v0
	v_and_b32_e32 v2, 7, v0
	v_lshrrev_b32_e32 v3, 3, v0
	v_lshlrev_b32_e32 v2, 10, v2
	v_lshl_add_u32 v2, v3, 4, v2
	v_add_u32_e32 v2, 0x4000, v2
	v_add_u32_e32 v3, 0x4000, v2
	s_add_u32 s0, s4, 0x4000
	s_addc_u32 s1, s5, 0
	s_add_u32 s8, s0, 0x34000
	s_addc_u32 s9, s1, 0
	s_mul_i32 s2, s11, 0xc000
	s_add_u32 s14, s0, s2
	s_addc_u32 s15, s1, 0
	s_add_u32 s14, s14, 0xa000
	s_addc_u32 s15, s15, 0
	global_load_dwordx4 v[4:7], v1, s[14:15]
	s_add_u32 s14, s8, s2
	s_addc_u32 s15, s9, 0
	s_add_u32 s14, s14, 0xa000
	s_addc_u32 s15, s15, 0
	global_load_dwordx4 v[8:11], v1, s[14:15]
	s_waitcnt vmcnt(0)
	ds_write_b128 v2, v[4:7]
	ds_write_b128 v2, v[8:11] offset:8192
	s_cmp_eq_u32 s11, 3
	s_cbranch_scc1 .Lgs_final
	s_cmp_eq_u32 s11, 1
	s_cbranch_scc1 .Lgs_l1
	s_load_dwordx2 s[14:15], s[36:37], 0x28
	s_add_i32 s10, s11, 1
	s_lshl_b32 s40, s10, 13
	s_mul_i32 s10, s10, 0xc000
	s_waitcnt lgkmcnt(0)
	s_add_u32 s14, s14, s40
	s_addc_u32 s15, s15, 0
	s_branch .Lgs_n1
.Lgs_l1:
	s_load_dwordx2 s[14:15], s[36:37], 0x68
	s_mov_b32 s10, 0x30000
	s_waitcnt lgkmcnt(0)
.Lgs_n1:
	global_load_dwordx4 v[4:7], v1, s[14:15]
	s_add_u32 s40, s0, s10
	s_addc_u32 s41, s1, 0
	global_load_dwordx4 v[8:11], v1, s[40:41]
	s_add_u32 s40, s40, 0x2000
	s_addc_u32 s41, s41, 0
	global_load_dwordx4 v[12:15], v1, s[40:41]
	s_add_u32 s40, s8, s10
	s_addc_u32 s41, s9, 0
	global_load_dwordx4 v[16:19], v1, s[40:41]
	s_add_u32 s40, s40, 0x2000
	s_addc_u32 s41, s41, 0
	global_load_dwordx4 v[20:23], v1, s[40:41]
	s_waitcnt vmcnt(0)
	v_add_f32_e32 v12, 1.0, v12
	v_add_f32_e32 v13, 1.0, v13
	v_add_f32_e32 v14, 1.0, v14
	v_add_f32_e32 v15, 1.0, v15
	v_mul_f32_e32 v12, v4, v12
	v_mul_f32_e32 v13, v5, v13
	v_mul_f32_e32 v14, v6, v14
	v_mul_f32_e32 v15, v7, v15
	ds_write_b128 v2, v[12:15] offset:16384
	ds_write_b128 v2, v[8:11] offset:24576
	v_add_f32_e32 v20, 1.0, v20
	v_add_f32_e32 v21, 1.0, v21
	v_add_f32_e32 v22, 1.0, v22
	v_add_f32_e32 v23, 1.0, v23
	v_mul_f32_e32 v20, v4, v20
	v_mul_f32_e32 v21, v5, v21
	v_mul_f32_e32 v22, v6, v22
	v_mul_f32_e32 v23, v7, v23
	ds_write_b128 v3, v[20:23] offset:16384
	ds_write_b128 v3, v[16:19] offset:24576
	s_cmp_eq_u32 s11, 1
	s_cbranch_scc0 .Lgs_done
	s_load_dwordx2 s[14:15], s[36:37], 0x28
	s_waitcnt lgkmcnt(0)
	s_add_u32 s14, s14, 0x4000
	s_addc_u32 s15, s15, 0
	global_load_dwordx4 v[4:7], v1, s[14:15]
	s_add_u32 s40, s0, 0x18000
	s_addc_u32 s41, s1, 0
	global_load_dwordx4 v[8:11], v1, s[40:41]
	s_add_u32 s40, s40, 0x2000
	s_addc_u32 s41, s41, 0
	global_load_dwordx4 v[12:15], v1, s[40:41]
	s_add_u32 s40, s8, 0x18000
	s_addc_u32 s41, s9, 0
	global_load_dwordx4 v[16:19], v1, s[40:41]
	s_add_u32 s40, s40, 0x2000
	s_addc_u32 s41, s41, 0
	global_load_dwordx4 v[20:23], v1, s[40:41]
	s_waitcnt vmcnt(0)
	v_add_f32_e32 v12, 1.0, v12
	v_add_f32_e32 v13, 1.0, v13
	v_add_f32_e32 v14, 1.0, v14
	v_add_f32_e32 v15, 1.0, v15
	v_mul_f32_e32 v12, v4, v12
	v_mul_f32_e32 v13, v5, v13
	v_mul_f32_e32 v14, v6, v14
	v_mul_f32_e32 v15, v7, v15
	ds_write_b128 v2, v[12:15] offset:49152
	ds_write_b128 v2, v[8:11] offset:57344
	v_add_f32_e32 v20, 1.0, v20
	v_add_f32_e32 v21, 1.0, v21
	v_add_f32_e32 v22, 1.0, v22
	v_add_f32_e32 v23, 1.0, v23
	v_mul_f32_e32 v20, v4, v20
	v_mul_f32_e32 v21, v5, v21
	v_mul_f32_e32 v22, v6, v22
	v_mul_f32_e32 v23, v7, v23
	ds_write_b128 v3, v[20:23] offset:49152
	ds_write_b128 v3, v[16:19] offset:57344
	s_branch .Lgs_done
.Lgs_final:
	s_load_dwordx2 s[14:15], s[36:37], 0xc8
	s_waitcnt lgkmcnt(0)
	global_load_dwordx4 v[4:7], v1, s[14:15]
	s_waitcnt vmcnt(0)
	ds_write_b128 v2, v[4:7] offset:16384
.Lgs_done:
	s_waitcnt lgkmcnt(0)
	s_barrier
	s_branch .LBB0_1405

.Lge_epi:
	s_ashr_i32 s2, s44, 13
	s_lshl_b64 s[0:1], s[44:45], 12
	v_lshl_add_u64 v[32:33], v[94:95], 0, s[0:1]
	global_load_dwordx4 v[0:3], v[32:33], off offset:0
	global_load_dwordx4 v[4:7], v[32:33], off offset:16
	global_load_dwordx4 v[8:11], v[32:33], off offset:32
	global_load_dwordx4 v[12:15], v[32:33], off offset:48
	v_lshlrev_b32_e32 v34, 4, v80
	v_add_u32_e32 v34, 0x4000, v34
	s_lshl_b32 s10, s2, 13
	v_add_u32_e32 v35, s10, v34
	ds_read_b128 v[36:39], v35 offset:0
	ds_read_b128 v[40:43], v35 offset:1024
	ds_read_b128 v[44:47], v35 offset:2048
	ds_read_b128 v[48:51], v35 offset:3072
	ds_read_b128 v[52:55], v35 offset:4096
	ds_read_b128 v[56:59], v35 offset:5120
	ds_read_b128 v[60:63], v35 offset:6144
	ds_read_b128 v[64:67], v35 offset:7168
	s_lshl_b32 s10, s2, 14
	v_add_u32_e32 v34, s10, v34
	s_waitcnt vmcnt(0) lgkmcnt(0)
	v_lshlrev_b32_e32 v70, 16, v0
	v_and_b32_e32 v71, 0xffff0000, v0
	v_pk_fma_f32 v[100:101], v[178:179], v[36:37], v[70:71]
	v_lshlrev_b32_e32 v70, 16, v1
	v_and_b32_e32 v71, 0xffff0000, v1
	v_pk_fma_f32 v[102:103], v[184:185], v[38:39], v[70:71]
	v_lshlrev_b32_e32 v70, 16, v2
	v_and_b32_e32 v71, 0xffff0000, v2
	v_pk_fma_f32 v[104:105], v[182:183], v[40:41], v[70:71]
	v_lshlrev_b32_e32 v70, 16, v3
	v_and_b32_e32 v71, 0xffff0000, v3
	v_pk_fma_f32 v[106:107], v[180:181], v[42:43], v[70:71]
	v_lshlrev_b32_e32 v70, 16, v4
	v_and_b32_e32 v71, 0xffff0000, v4
	v_pk_fma_f32 v[108:109], v[176:177], v[44:45], v[70:71]
	v_lshlrev_b32_e32 v70, 16, v5
	v_and_b32_e32 v71, 0xffff0000, v5
	v_pk_fma_f32 v[110:111], v[174:175], v[46:47], v[70:71]
	v_lshlrev_b32_e32 v70, 16, v6
	v_and_b32_e32 v71, 0xffff0000, v6
	v_pk_fma_f32 v[112:113], v[160:161], v[48:49], v[70:71]
	v_lshlrev_b32_e32 v70, 16, v7
	v_and_b32_e32 v71, 0xffff0000, v7
	v_pk_fma_f32 v[114:115], v[158:159], v[50:51], v[70:71]
	v_lshlrev_b32_e32 v70, 16, v8
	v_and_b32_e32 v71, 0xffff0000, v8
	v_pk_fma_f32 v[116:117], v[156:157], v[52:53], v[70:71]
	v_lshlrev_b32_e32 v70, 16, v9
	v_and_b32_e32 v71, 0xffff0000, v9
	v_pk_fma_f32 v[118:119], v[154:155], v[54:55], v[70:71]
	v_lshlrev_b32_e32 v70, 16, v10
	v_and_b32_e32 v71, 0xffff0000, v10
	v_pk_fma_f32 v[120:121], v[152:153], v[56:57], v[70:71]
	v_lshlrev_b32_e32 v70, 16, v11
	v_and_b32_e32 v71, 0xffff0000, v11
	v_pk_fma_f32 v[122:123], v[150:151], v[58:59], v[70:71]
	v_lshlrev_b32_e32 v70, 16, v12
	v_and_b32_e32 v71, 0xffff0000, v12
	v_pk_fma_f32 v[124:125], v[148:149], v[60:61], v[70:71]
	v_lshlrev_b32_e32 v70, 16, v13
	v_and_b32_e32 v71, 0xffff0000, v13
	v_pk_fma_f32 v[126:127], v[146:147], v[62:63], v[70:71]
	v_lshlrev_b32_e32 v70, 16, v14
	v_and_b32_e32 v71, 0xffff0000, v14
	v_pk_fma_f32 v[128:129], v[144:145], v[64:65], v[70:71]
	v_lshlrev_b32_e32 v70, 16, v15
	v_and_b32_e32 v71, 0xffff0000, v15
	v_pk_fma_f32 v[130:131], v[142:143], v[66:67], v[70:71]
	v_pk_mul_f32 v[72:73], v[100:101], v[100:101]
	v_pk_fma_f32 v[72:73], v[102:103], v[102:103], v[72:73]
	v_pk_fma_f32 v[72:73], v[104:105], v[104:105], v[72:73]
	v_pk_fma_f32 v[72:73], v[106:107], v[106:107], v[72:73]
	v_pk_fma_f32 v[72:73], v[108:109], v[108:109], v[72:73]
	v_pk_fma_f32 v[72:73], v[110:111], v[110:111], v[72:73]
	v_pk_fma_f32 v[72:73], v[112:113], v[112:113], v[72:73]
	v_pk_fma_f32 v[72:73], v[114:115], v[114:115], v[72:73]
	v_pk_fma_f32 v[72:73], v[116:117], v[116:117], v[72:73]
	v_pk_fma_f32 v[72:73], v[118:119], v[118:119], v[72:73]
	v_pk_fma_f32 v[72:73], v[120:121], v[120:121], v[72:73]
	v_pk_fma_f32 v[72:73], v[122:123], v[122:123], v[72:73]
	v_pk_fma_f32 v[72:73], v[124:125], v[124:125], v[72:73]
	v_pk_fma_f32 v[72:73], v[126:127], v[126:127], v[72:73]
	v_pk_fma_f32 v[72:73], v[128:129], v[128:129], v[72:73]
	v_pk_fma_f32 v[72:73], v[130:131], v[130:131], v[72:73]
	v_add_f32_e32 v72, v72, v73
	s_and_b64 vcc, exec, s[52:53]
	s_cbranch_vccz .Lge_noxc
	v_cvt_pk_bf16_f32 v0, v100, v101
	v_cvt_pk_bf16_f32 v1, v102, v103
	v_cvt_pk_bf16_f32 v2, v104, v105
	v_cvt_pk_bf16_f32 v3, v106, v107
	v_cvt_pk_bf16_f32 v4, v108, v109
	v_cvt_pk_bf16_f32 v5, v110, v111
	v_cvt_pk_bf16_f32 v6, v112, v113
	v_cvt_pk_bf16_f32 v7, v114, v115
	v_cvt_pk_bf16_f32 v8, v116, v117
	v_cvt_pk_bf16_f32 v9, v118, v119
	v_cvt_pk_bf16_f32 v10, v120, v121
	v_cvt_pk_bf16_f32 v11, v122, v123
	v_cvt_pk_bf16_f32 v12, v124, v125
	v_cvt_pk_bf16_f32 v13, v126, v127
	v_cvt_pk_bf16_f32 v14, v128, v129
	v_cvt_pk_bf16_f32 v15, v130, v131
	global_store_dwordx4 v[32:33], v[0:3], off offset:0
	global_store_dwordx4 v[32:33], v[4:7], off offset:16
	global_store_dwordx4 v[32:33], v[8:11], off offset:32
	global_store_dwordx4 v[32:33], v[12:15], off offset:48
.Lge_noxc:
	v_mov_b32_e32 v73, v97
	s_nop 0
	v_add_f32_dpp v72, v72, v72 quad_perm:[1,0,3,2] row_mask:0xf bank_mask:0xf bound_ctrl:1
	s_nop 1
	v_add_f32_dpp v72, v72, v72 quad_perm:[2,3,0,1] row_mask:0xf bank_mask:0xf bound_ctrl:1
	s_nop 1
	v_add_f32_dpp v72, v72, v72 row_half_mirror row_mask:0xf bank_mask:0xf bound_ctrl:1
	s_nop 1
	v_add_f32_dpp v72, v72, v72 row_mirror row_mask:0xf bank_mask:0xf bound_ctrl:1
	s_nop 1
	v_mov_b32_dpp v73, v72 row_bcast:15 row_mask:0xa bank_mask:0xf
	v_add_f32_e32 v72, v72, v73
	v_mov_b32_e32 v73, v97
	s_nop 1
	v_mov_b32_dpp v73, v72 row_bcast:31 row_mask:0xc bank_mask:0xf
	v_add_f32_e32 v72, v72, v73
	s_nop 0
	v_readlane_b32 s4, v72, 63
	s_nop 1
	v_fma_f32 v32, s4, v217, v205
	v_mul_f32_e32 v33, 0x4b800000, v32
	v_cmp_gt_f32_e32 vcc, s17, v32
	s_nop 1
	v_cndmask_b32_e32 v32, v32, v33, vcc
	v_rsq_f32_e32 v32, v32
	s_nop 0
	v_mul_f32_e32 v33, 0x45800000, v32
	v_cndmask_b32_e32 v32, v32, v33, vcc
	s_and_b64 vcc, exec, s[52:53]
	s_cbranch_vccz .Lge_final
	ds_read_b128 v[36:39], v34 offset:16384
	ds_read_b128 v[40:43], v34 offset:17408
	ds_read_b128 v[44:47], v34 offset:18432
	ds_read_b128 v[48:51], v34 offset:19456
	ds_read_b128 v[52:55], v34 offset:20480
	ds_read_b128 v[56:59], v34 offset:21504
	ds_read_b128 v[60:63], v34 offset:22528
	ds_read_b128 v[64:67], v34 offset:23552
	ds_read_b128 v[0:3], v34 offset:24576
	ds_read_b128 v[4:7], v34 offset:25600
	ds_read_b128 v[8:11], v34 offset:26624
	ds_read_b128 v[12:15], v34 offset:27648
	ds_read_b128 v[16:19], v34 offset:28672
	ds_read_b128 v[20:23], v34 offset:29696
	ds_read_b128 v[24:27], v34 offset:30720
	ds_read_b128 v[28:31], v34 offset:31744
	s_waitcnt lgkmcnt(0)
	v_pk_mul_f32 v[36:37], v[36:37], v[32:33] op_sel_hi:[1,0]
	v_pk_mul_f32 v[38:39], v[38:39], v[32:33] op_sel_hi:[1,0]
	v_pk_mul_f32 v[40:41], v[40:41], v[32:33] op_sel_hi:[1,0]
	v_pk_mul_f32 v[42:43], v[42:43], v[32:33] op_sel_hi:[1,0]
	v_pk_mul_f32 v[44:45], v[44:45], v[32:33] op_sel_hi:[1,0]
	v_pk_mul_f32 v[46:47], v[46:47], v[32:33] op_sel_hi:[1,0]
	v_pk_mul_f32 v[48:49], v[48:49], v[32:33] op_sel_hi:[1,0]
	v_pk_mul_f32 v[50:51], v[50:51], v[32:33] op_sel_hi:[1,0]
	v_pk_mul_f32 v[52:53], v[52:53], v[32:33] op_sel_hi:[1,0]
	v_pk_mul_f32 v[54:55], v[54:55], v[32:33] op_sel_hi:[1,0]
	v_pk_mul_f32 v[56:57], v[56:57], v[32:33] op_sel_hi:[1,0]
	v_pk_mul_f32 v[58:59], v[58:59], v[32:33] op_sel_hi:[1,0]
	v_pk_mul_f32 v[60:61], v[60:61], v[32:33] op_sel_hi:[1,0]
	v_pk_mul_f32 v[62:63], v[62:63], v[32:33] op_sel_hi:[1,0]
	v_pk_mul_f32 v[64:65], v[64:65], v[32:33] op_sel_hi:[1,0]
	v_pk_mul_f32 v[66:67], v[66:67], v[32:33] op_sel_hi:[1,0]
	v_pk_fma_f32 v[0:1], v[100:101], v[36:37], v[0:1]
	v_pk_fma_f32 v[2:3], v[102:103], v[38:39], v[2:3]
	v_pk_fma_f32 v[4:5], v[104:105], v[40:41], v[4:5]
	v_pk_fma_f32 v[6:7], v[106:107], v[42:43], v[6:7]
	v_pk_fma_f32 v[8:9], v[108:109], v[44:45], v[8:9]
	v_pk_fma_f32 v[10:11], v[110:111], v[46:47], v[10:11]
	v_pk_fma_f32 v[12:13], v[112:113], v[48:49], v[12:13]
	v_pk_fma_f32 v[14:15], v[114:115], v[50:51], v[14:15]
	v_pk_fma_f32 v[16:17], v[116:117], v[52:53], v[16:17]
	v_pk_fma_f32 v[18:19], v[118:119], v[54:55], v[18:19]
	v_pk_fma_f32 v[20:21], v[120:121], v[56:57], v[20:21]
	v_pk_fma_f32 v[22:23], v[122:123], v[58:59], v[22:23]
	v_pk_fma_f32 v[24:25], v[124:125], v[60:61], v[24:25]
	v_pk_fma_f32 v[26:27], v[126:127], v[62:63], v[26:27]
	v_pk_fma_f32 v[28:29], v[128:129], v[64:65], v[28:29]
	v_pk_fma_f32 v[30:31], v[130:131], v[66:67], v[30:31]
	v_cvt_pk_bf16_f32 v36, v0, v1
	v_cvt_pk_bf16_f32 v37, v2, v3
	v_cvt_pk_bf16_f32 v38, v4, v5
	v_cvt_pk_bf16_f32 v39, v6, v7
	v_cvt_pk_bf16_f32 v40, v8, v9
	v_cvt_pk_bf16_f32 v41, v10, v11
	v_cvt_pk_bf16_f32 v42, v12, v13
	v_cvt_pk_bf16_f32 v43, v14, v15
	v_cvt_pk_bf16_f32 v44, v16, v17
	v_cvt_pk_bf16_f32 v45, v18, v19
	v_cvt_pk_bf16_f32 v46, v20, v21
	v_cvt_pk_bf16_f32 v47, v22, v23
	v_cvt_pk_bf16_f32 v48, v24, v25
	v_cvt_pk_bf16_f32 v49, v26, v27
	v_cvt_pk_bf16_f32 v50, v28, v29
	v_cvt_pk_bf16_f32 v51, v30, v31
	v_lshl_add_u64 v[68:69], v[84:85], 0, s[0:1]
	global_store_dwordx4 v[68:69], v[36:39], off offset:0
	global_store_dwordx4 v[68:69], v[40:43], off offset:16
	global_store_dwordx4 v[68:69], v[44:47], off offset:32
	global_store_dwordx4 v[68:69], v[48:51], off offset:48
	s_nop 1
	s_and_b64 vcc, exec, s[54:55]
	s_cbranch_vccz .LBB0_1404
	ds_read_b128 v[36:39], v34 offset:49152
	ds_read_b128 v[40:43], v34 offset:50176
	ds_read_b128 v[44:47], v34 offset:51200
	ds_read_b128 v[48:51], v34 offset:52224
	ds_read_b128 v[52:55], v34 offset:53248
	ds_read_b128 v[56:59], v34 offset:54272
	ds_read_b128 v[60:63], v34 offset:55296
	ds_read_b128 v[64:67], v34 offset:56320
	ds_read_b128 v[0:3], v34 offset:57344
	ds_read_b128 v[4:7], v34 offset:58368
	ds_read_b128 v[8:11], v34 offset:59392
	ds_read_b128 v[12:15], v34 offset:60416
	ds_read_b128 v[16:19], v34 offset:61440
	ds_read_b128 v[20:23], v34 offset:62464
	ds_read_b128 v[24:27], v34 offset:63488
	ds_read_b128 v[28:31], v34 offset:64512
	s_waitcnt lgkmcnt(0)
	v_pk_mul_f32 v[36:37], v[36:37], v[32:33] op_sel_hi:[1,0]
	v_pk_mul_f32 v[38:39], v[38:39], v[32:33] op_sel_hi:[1,0]
	v_pk_mul_f32 v[40:41], v[40:41], v[32:33] op_sel_hi:[1,0]
	v_pk_mul_f32 v[42:43], v[42:43], v[32:33] op_sel_hi:[1,0]
	v_pk_mul_f32 v[44:45], v[44:45], v[32:33] op_sel_hi:[1,0]
	v_pk_mul_f32 v[46:47], v[46:47], v[32:33] op_sel_hi:[1,0]
	v_pk_mul_f32 v[48:49], v[48:49], v[32:33] op_sel_hi:[1,0]
	v_pk_mul_f32 v[50:51], v[50:51], v[32:33] op_sel_hi:[1,0]
	v_pk_mul_f32 v[52:53], v[52:53], v[32:33] op_sel_hi:[1,0]
	v_pk_mul_f32 v[54:55], v[54:55], v[32:33] op_sel_hi:[1,0]
	v_pk_mul_f32 v[56:57], v[56:57], v[32:33] op_sel_hi:[1,0]
	v_pk_mul_f32 v[58:59], v[58:59], v[32:33] op_sel_hi:[1,0]
	v_pk_mul_f32 v[60:61], v[60:61], v[32:33] op_sel_hi:[1,0]
	v_pk_mul_f32 v[62:63], v[62:63], v[32:33] op_sel_hi:[1,0]
	v_pk_mul_f32 v[64:65], v[64:65], v[32:33] op_sel_hi:[1,0]
	v_pk_mul_f32 v[66:67], v[66:67], v[32:33] op_sel_hi:[1,0]
	v_pk_fma_f32 v[0:1], v[100:101], v[36:37], v[0:1]
	v_pk_fma_f32 v[2:3], v[102:103], v[38:39], v[2:3]
	v_pk_fma_f32 v[4:5], v[104:105], v[40:41], v[4:5]
	v_pk_fma_f32 v[6:7], v[106:107], v[42:43], v[6:7]
	v_pk_fma_f32 v[8:9], v[108:109], v[44:45], v[8:9]
	v_pk_fma_f32 v[10:11], v[110:111], v[46:47], v[10:11]
	v_pk_fma_f32 v[12:13], v[112:113], v[48:49], v[12:13]
	v_pk_fma_f32 v[14:15], v[114:115], v[50:51], v[14:15]
	v_pk_fma_f32 v[16:17], v[116:117], v[52:53], v[16:17]
	v_pk_fma_f32 v[18:19], v[118:119], v[54:55], v[18:19]
	v_pk_fma_f32 v[20:21], v[120:121], v[56:57], v[20:21]
	v_pk_fma_f32 v[22:23], v[122:123], v[58:59], v[22:23]
	v_pk_fma_f32 v[24:25], v[124:125], v[60:61], v[24:25]
	v_pk_fma_f32 v[26:27], v[126:127], v[62:63], v[26:27]
	v_pk_fma_f32 v[28:29], v[128:129], v[64:65], v[28:29]
	v_pk_fma_f32 v[30:31], v[130:131], v[66:67], v[30:31]
	v_cvt_pk_bf16_f32 v36, v0, v1
	v_cvt_pk_bf16_f32 v37, v2, v3
	v_cvt_pk_bf16_f32 v38, v4, v5
	v_cvt_pk_bf16_f32 v39, v6, v7
	v_cvt_pk_bf16_f32 v40, v8, v9
	v_cvt_pk_bf16_f32 v41, v10, v11
	v_cvt_pk_bf16_f32 v42, v12, v13
	v_cvt_pk_bf16_f32 v43, v14, v15
	v_cvt_pk_bf16_f32 v44, v16, v17
	v_cvt_pk_bf16_f32 v45, v18, v19
	v_cvt_pk_bf16_f32 v46, v20, v21
	v_cvt_pk_bf16_f32 v47, v22, v23
	v_cvt_pk_bf16_f32 v48, v24, v25
	v_cvt_pk_bf16_f32 v49, v26, v27
	v_cvt_pk_bf16_f32 v50, v28, v29
	v_cvt_pk_bf16_f32 v51, v30, v31
	v_lshl_add_u64 v[68:69], v[86:87], 0, s[0:1]
	global_store_dwordx4 v[68:69], v[36:39], off offset:0
	global_store_dwordx4 v[68:69], v[40:43], off offset:16
	global_store_dwordx4 v[68:69], v[44:47], off offset:32
	global_store_dwordx4 v[68:69], v[48:51], off offset:48
	s_nop 1
	s_branch .LBB0_1404
.Lge_final:
	s_load_dwordx2 s[40:41], s[36:37], 0xd0
	v_lshlrev_b32_e32 v34, 4, v80
	v_add_u32_e32 v34, 0x4000, v34
	ds_read_b128 v[36:39], v34 offset:16384
	ds_read_b128 v[40:43], v34 offset:17408
	ds_read_b128 v[44:47], v34 offset:18432
	ds_read_b128 v[48:51], v34 offset:19456
	ds_read_b128 v[52:55], v34 offset:20480
	ds_read_b128 v[56:59], v34 offset:21504
	ds_read_b128 v[60:63], v34 offset:22528
	ds_read_b128 v[64:67], v34 offset:23552
	s_lshl_b64 s[0:1], s[44:45], 13
	v_lshlrev_b32_e32 v35, 7, v80
	s_waitcnt lgkmcnt(0)
	s_add_u32 s0, s40, s0
	s_addc_u32 s1, s41, s1
	v_pk_mul_f32 v[100:101], v[100:101], v[32:33] op_sel_hi:[1,0]
	v_pk_mul_f32 v[102:103], v[102:103], v[32:33] op_sel_hi:[1,0]
	v_pk_mul_f32 v[104:105], v[104:105], v[32:33] op_sel_hi:[1,0]
	v_pk_mul_f32 v[106:107], v[106:107], v[32:33] op_sel_hi:[1,0]
	v_pk_mul_f32 v[108:109], v[108:109], v[32:33] op_sel_hi:[1,0]
	v_pk_mul_f32 v[110:111], v[110:111], v[32:33] op_sel_hi:[1,0]
	v_pk_mul_f32 v[112:113], v[112:113], v[32:33] op_sel_hi:[1,0]
	v_pk_mul_f32 v[114:115], v[114:115], v[32:33] op_sel_hi:[1,0]
	v_pk_mul_f32 v[116:117], v[116:117], v[32:33] op_sel_hi:[1,0]
	v_pk_mul_f32 v[118:119], v[118:119], v[32:33] op_sel_hi:[1,0]
	v_pk_mul_f32 v[120:121], v[120:121], v[32:33] op_sel_hi:[1,0]
	v_pk_mul_f32 v[122:123], v[122:123], v[32:33] op_sel_hi:[1,0]
	v_pk_mul_f32 v[124:125], v[124:125], v[32:33] op_sel_hi:[1,0]
	v_pk_mul_f32 v[126:127], v[126:127], v[32:33] op_sel_hi:[1,0]
	v_pk_mul_f32 v[128:129], v[128:129], v[32:33] op_sel_hi:[1,0]
	v_pk_mul_f32 v[130:131], v[130:131], v[32:33] op_sel_hi:[1,0]
	v_pk_mul_f32 v[100:101], v[100:101], v[36:37]
	v_pk_mul_f32 v[102:103], v[102:103], v[38:39]
	v_pk_mul_f32 v[104:105], v[104:105], v[40:41]
	v_pk_mul_f32 v[106:107], v[106:107], v[42:43]
	v_pk_mul_f32 v[108:109], v[108:109], v[44:45]
	v_pk_mul_f32 v[110:111], v[110:111], v[46:47]
	v_pk_mul_f32 v[112:113], v[112:113], v[48:49]
	v_pk_mul_f32 v[114:115], v[114:115], v[50:51]
	v_pk_mul_f32 v[116:117], v[116:117], v[52:53]
	v_pk_mul_f32 v[118:119], v[118:119], v[54:55]
	v_pk_mul_f32 v[120:121], v[120:121], v[56:57]
	v_pk_mul_f32 v[122:123], v[122:123], v[58:59]
	v_pk_mul_f32 v[124:125], v[124:125], v[60:61]
	v_pk_mul_f32 v[126:127], v[126:127], v[62:63]
	v_pk_mul_f32 v[128:129], v[128:129], v[64:65]
	v_pk_mul_f32 v[130:131], v[130:131], v[66:67]
	global_store_dwordx4 v35, v[100:103], s[0:1] offset:0
	global_store_dwordx4 v35, v[104:107], s[0:1] offset:16
	global_store_dwordx4 v35, v[108:111], s[0:1] offset:32
	global_store_dwordx4 v35, v[112:115], s[0:1] offset:48
	global_store_dwordx4 v35, v[116:119], s[0:1] offset:64
	global_store_dwordx4 v35, v[120:123], s[0:1] offset:80
	global_store_dwordx4 v35, v[124:127], s[0:1] offset:96
	global_store_dwordx4 v35, v[128:131], s[0:1] offset:112
	s_nop 1
	s_branch .LBB0_1404
